# k31 + XCD leaders no longer wait for the acks of their relay/TOPGEN atomics before leaving the barrier
# speedup vs baseline: 1.0003x; 1.0003x over previous
; __device__ __forceinline__ unsigned xb_add(unsigned* p, unsigned v) { return __hip_atomic_fetch_add(p, v, __ATOMIC_RELAXED, __HIP_MEMORY_SCOPE_AGENT); }
; __device__ __forceinline__ void xcd_barrier(const XcdBarrier& b) {
;     ...
;             __builtin_amdgcn_fence(__ATOMIC_ACQUIRE, "agent");
;             xb_add(&bar[XB_XGEN(b.x)], 1u);
;             asm volatile("s_waitcnt vmcnt(0)" ::: "memory");
.LBB0_96:
	s_or_b64 exec, exec, s[4:5]
	v_mov_b32_e32 v1, 0x2000
	v_add_u32_e32 v2, 1, v4
	global_atomic_umax v1, v2, s[2:3] offset:1024

; __device__ __forceinline__ unsigned xb_add(unsigned* p, unsigned v) { return __hip_atomic_fetch_add(p, v, __ATOMIC_RELAXED, __HIP_MEMORY_SCOPE_AGENT); }
; __device__ __forceinline__ void xcd_barrier(const XcdBarrier& b) {
;     ...
;             __builtin_amdgcn_fence(__ATOMIC_ACQUIRE, "agent");
;             xb_add(&bar[XB_XGEN(b.x)], 1u);
;             asm volatile("s_waitcnt vmcnt(0)" ::: "memory");
.LBB0_257:
	s_or_b64 exec, exec, s[4:5]
	v_mov_b32_e32 v2, 0x2000
	v_add_u32_e32 v3, 1, v4
	global_atomic_umax v2, v3, s[2:3] offset:1024

; __device__ __forceinline__ unsigned xb_add(unsigned* p, unsigned v) { return __hip_atomic_fetch_add(p, v, __ATOMIC_RELAXED, __HIP_MEMORY_SCOPE_AGENT); }
; __device__ __forceinline__ void xcd_barrier(const XcdBarrier& b) {
;     ...
;             __builtin_amdgcn_fence(__ATOMIC_ACQUIRE, "agent");
;             xb_add(&bar[XB_XGEN(b.x)], 1u);
;             asm volatile("s_waitcnt vmcnt(0)" ::: "memory");
.LBB0_4462:
	s_or_b64 exec, exec, s[4:5]
	v_mov_b32_e32 v1, 0x2000
	v_add_u32_e32 v2, 1, v4
	global_atomic_umax v1, v2, s[0:1] offset:1024
